# speedup vs baseline: 1.0124x; 1.0036x over previous
.Llight_path:
	s_waitcnt vmcnt(16)
	v_mul_u32_u24_e32 v236, 36, v228
	v_add_u32_e32 v236, v236, v230
	v_add_u32_e32 v237, s7, v229
	v_mul_u32_u24_e32 v238, 0x104, v228
	v_add_u32_e32 v238, v238, v237
	v_add_u32_e32 v238, 0xb840, v238
	v_add_u32_e32 v231, s7, v229
	v_add_u32_e32 v231, 0xb840, v231
	v_add_u32_e32 v211, s6, v210
	s_nop 0
	s_load_dwordx8 s[4:11], s[0:1], 0x10
	v_add_u32_e32 v232, 0x24e80, v228
	ds_read_b32 v244, v232
	ds_read_b32 v245, v232 offset:128
	ds_read_b128 v[194:197], v237 offset:36928
	ds_read_b128 v[198:201], v237 offset:36944
	ds_read_b128 v[202:205], v237 offset:36960
	ds_read_b128 v[206:209], v237 offset:36976
	ds_read_b128 v[212:215], v237 offset:37056
	ds_read_b128 v[216:219], v237 offset:37072
	ds_read_b128 v[220:223], v237 offset:37088
	ds_read_b128 v[224:227], v237 offset:37104
	ds_read_b128 v[162:165], v236 offset:16384
	ds_read_b128 v[166:169], v236 offset:16416
	ds_read_b128 v[170:173], v236 offset:16448
	ds_read_b128 v[174:177], v236 offset:16480
	s_waitcnt lgkmcnt(0)
	v_mfma_f32_32x32x16_bf16 v[2:17], v[94:97], v[162:165], v[194:209]
	v_mfma_f32_32x32x16_bf16 v[18:33], v[46:49], v[162:165], v[212:227]
	v_mfma_f32_32x32x16_bf16 v[2:17], v[90:93], v[166:169], v[2:17]
	v_mfma_f32_32x32x16_bf16 v[18:33], v[42:45], v[166:169], v[18:33]
	v_mfma_f32_32x32x16_bf16 v[2:17], v[86:89], v[170:173], v[2:17]
	ds_read_b128 v[178:181], v236 offset:20992
	v_mfma_f32_32x32x16_bf16 v[18:33], v[38:41], v[170:173], v[18:33]
	ds_read_b128 v[182:185], v236 offset:21024
	v_mfma_f32_32x32x16_bf16 v[2:17], v[82:85], v[174:177], v[2:17]
	ds_read_b128 v[186:189], v236 offset:21056
	v_mfma_f32_32x32x16_bf16 v[18:33], v[34:37], v[174:177], v[18:33]
	ds_read_b128 v[190:193], v236 offset:21088
	s_waitcnt lgkmcnt(0)
	v_mfma_f32_32x32x16_bf16 v[130:145], v[94:97], v[178:181], v[194:209]
	v_mfma_f32_32x32x16_bf16 v[146:161], v[46:49], v[178:181], v[212:227]
	v_mfma_f32_32x32x16_bf16 v[130:145], v[90:93], v[182:185], v[130:145]
	v_mfma_f32_32x32x16_bf16 v[146:161], v[42:45], v[182:185], v[146:161]
	s_nop 7
	ds_write_b128 v238, v[2:5] offset:0
	ds_write_b128 v238, v[6:9] offset:16
	ds_write_b128 v238, v[10:13] offset:32
	ds_write_b128 v238, v[14:17] offset:48
	ds_write_b128 v238, v[18:21] offset:128
	ds_write_b128 v238, v[22:25] offset:144
	ds_write_b128 v238, v[26:29] offset:160
	ds_write_b128 v238, v[30:33] offset:176
	v_mfma_f32_32x32x16_bf16 v[130:145], v[86:89], v[186:189], v[130:145]
	ds_read_b128 v[162:165], v236 offset:25600
	v_mfma_f32_32x32x16_bf16 v[146:161], v[38:41], v[186:189], v[146:161]
	ds_read_b128 v[166:169], v236 offset:25632
	v_mfma_f32_32x32x16_bf16 v[130:145], v[82:85], v[190:193], v[130:145]
	ds_read_b128 v[170:173], v236 offset:25664
	v_mfma_f32_32x32x16_bf16 v[146:161], v[34:37], v[190:193], v[146:161]
	ds_read_b128 v[174:177], v236 offset:25696
	s_waitcnt lgkmcnt(0)
	v_mfma_f32_32x32x16_bf16 v[2:17], v[94:97], v[162:165], v[194:209]
	v_mfma_f32_32x32x16_bf16 v[18:33], v[46:49], v[162:165], v[212:227]
	v_mfma_f32_32x32x16_bf16 v[2:17], v[90:93], v[166:169], v[2:17]
	v_mfma_f32_32x32x16_bf16 v[18:33], v[42:45], v[166:169], v[18:33]
	s_nop 7
	v_add_u32_e32 v239, 0x8200, v238
	ds_write_b128 v239, v[130:133] offset:0
	ds_write_b128 v239, v[134:137] offset:16
	ds_write_b128 v239, v[138:141] offset:32
	ds_write_b128 v239, v[142:145] offset:48
	ds_write_b128 v239, v[146:149] offset:128
	ds_write_b128 v239, v[150:153] offset:144
	ds_write_b128 v239, v[154:157] offset:160
	ds_write_b128 v239, v[158:161] offset:176
	v_mfma_f32_32x32x16_bf16 v[2:17], v[86:89], v[170:173], v[2:17]
	ds_read_b128 v[178:181], v236 offset:30208
	v_mfma_f32_32x32x16_bf16 v[18:33], v[38:41], v[170:173], v[18:33]
	ds_read_b128 v[182:185], v236 offset:30240
	v_mfma_f32_32x32x16_bf16 v[2:17], v[82:85], v[174:177], v[2:17]
	ds_read_b128 v[186:189], v236 offset:30272
	v_mfma_f32_32x32x16_bf16 v[18:33], v[34:37], v[174:177], v[18:33]
	ds_read_b128 v[190:193], v236 offset:30304
	s_waitcnt lgkmcnt(0)
	v_mfma_f32_32x32x16_bf16 v[130:145], v[94:97], v[178:181], v[194:209]
	v_mfma_f32_32x32x16_bf16 v[146:161], v[46:49], v[178:181], v[212:227]
	v_mfma_f32_32x32x16_bf16 v[130:145], v[90:93], v[182:185], v[130:145]
	v_mfma_f32_32x32x16_bf16 v[146:161], v[42:45], v[182:185], v[146:161]
	s_nop 7
	v_add_u32_e32 v239, 0x10400, v238
	ds_write_b128 v239, v[2:5] offset:0
	ds_write_b128 v239, v[6:9] offset:16
	ds_write_b128 v239, v[10:13] offset:32
	ds_write_b128 v239, v[14:17] offset:48
	ds_write_b128 v239, v[18:21] offset:128
	ds_write_b128 v239, v[22:25] offset:144
	ds_write_b128 v239, v[26:29] offset:160
	ds_write_b128 v239, v[30:33] offset:176
	v_mfma_f32_32x32x16_bf16 v[130:145], v[86:89], v[186:189], v[130:145]
	v_mfma_f32_32x32x16_bf16 v[146:161], v[38:41], v[186:189], v[146:161]
	v_mfma_f32_32x32x16_bf16 v[130:145], v[82:85], v[190:193], v[130:145]
	v_mfma_f32_32x32x16_bf16 v[146:161], v[34:37], v[190:193], v[146:161]
	s_nop 7
	s_nop 7
	v_cmp_gt_u32_e32 vcc, 16, v228
	s_and_saveexec_b64 s[20:21], vcc
	v_add_u32_e32 v239, 0x18600, v238
	ds_write_b128 v239, v[130:133] offset:0
	ds_write_b128 v239, v[134:137] offset:16
	ds_write_b128 v239, v[138:141] offset:32
	ds_write_b128 v239, v[142:145] offset:48
	ds_write_b128 v239, v[146:149] offset:128
	ds_write_b128 v239, v[150:153] offset:144
	ds_write_b128 v239, v[154:157] offset:160
	ds_write_b128 v239, v[158:161] offset:176
	s_or_b64 exec, exec, s[20:21]
	s_mov_b32 s12, 0xbeb17218
	v_mov_b32_e32 v235, 0xc038aa3b
	v_add_u32_e32 v233, v231, v244
	v_add_u32_e32 v234, v231, v245
	ds_read_b128 v[2:5], v233 offset:0
	ds_read_b128 v[6:9], v233 offset:16
	ds_read_b128 v[10:13], v233 offset:32
	ds_read_b128 v[14:17], v233 offset:48
	ds_read_b128 v[18:21], v233 offset:128
	ds_read_b128 v[22:25], v233 offset:144
	ds_read_b128 v[26:29], v233 offset:160
	ds_read_b128 v[30:33], v233 offset:176
	ds_read_b128 v[34:37], v234 offset:0
	ds_read_b128 v[38:41], v234 offset:16
	ds_read_b128 v[42:45], v234 offset:32
	ds_read_b128 v[46:49], v234 offset:48
	v_mov_b32_e32 v194, 0
	v_mov_b32_e32 v195, 0
	v_mov_b32_e32 v196, 0
	v_mov_b32_e32 v197, 0
	v_mov_b32_e32 v198, 0
	v_mov_b32_e32 v199, 0
	v_mov_b32_e32 v200, 0
	v_mov_b32_e32 v201, 0
	v_mov_b32_e32 v202, 0
	v_mov_b32_e32 v203, 0
	v_mov_b32_e32 v204, 0
	v_mov_b32_e32 v205, 0
	v_mov_b32_e32 v206, 0
	v_mov_b32_e32 v207, 0
	v_mov_b32_e32 v208, 0
	v_mov_b32_e32 v209, 0
	v_add_u32_e32 v232, 0x100, v232
	s_movk_i32 s16, 18
	s_waitcnt vmcnt(0) lgkmcnt(0)
	ds_read_b128 v[82:85], v234 offset:128
	ds_read_b128 v[86:89], v234 offset:144
	ds_read_b128 v[90:93], v234 offset:160
	ds_read_b128 v[94:97], v234 offset:176
	ds_read2_b32 v[244:245], v232 offset1:32
	v_exp_f32_e32 v212, v4
	v_exp_f32_e32 v213, v8
	v_exp_f32_e32 v214, v12
	v_exp_f32_e32 v215, v16
	v_exp_f32_e32 v217, v2
	v_fma_f32 v251, v212, s12, s12
	v_exp_f32_e32 v218, v6
	v_fma_f32 v252, v213, s12, s12
	v_exp_f32_e32 v219, v10
	v_fma_f32 v253, v214, s12, s12
	v_exp_f32_e32 v220, v14
	v_fma_f32 v254, v215, s12, s12
	v_fmac_f32_e32 v251, v217, v251
	v_fmac_f32_e32 v252, v218, v252
	v_fmac_f32_e32 v253, v219, v253
	v_fmac_f32_e32 v254, v220, v254
	v_rcp_f32_e32 v217, v251
	v_rcp_f32_e32 v218, v252
	v_rcp_f32_e32 v219, v253
	v_rcp_f32_e32 v220, v254
	v_exp_f32_e32 v246, v5
	v_fma_f32 v194, -v212, v217, v217
	v_exp_f32_e32 v247, v9
	v_fma_f32 v195, -v213, v218, v218
	v_exp_f32_e32 v248, v13
	v_fma_f32 v196, -v214, v219, v219
	v_exp_f32_e32 v249, v17
	v_fma_f32 v197, -v215, v220, v220
	v_exp_f32_e32 v212, v194
	v_add_f32_e32 v246, 1.0, v246
	v_exp_f32_e32 v213, v195
	v_add_f32_e32 v247, 1.0, v247
	v_exp_f32_e32 v214, v196
	v_add_f32_e32 v248, 1.0, v248
	v_exp_f32_e32 v215, v197
	v_add_f32_e32 v249, 1.0, v249
	v_fmac_f32_e32 v246, v246, v212
	v_fmac_f32_e32 v247, v247, v213
	v_fmac_f32_e32 v248, v248, v214
	v_fmac_f32_e32 v249, v249, v215
	v_rcp_f32_e32 v246, v246
	v_rcp_f32_e32 v247, v247
	v_rcp_f32_e32 v248, v248
	v_rcp_f32_e32 v249, v249
	v_fma_f32 v246, -v212, v246, v246
	v_fma_f32 v247, -v213, v247, v247
	v_fma_f32 v248, -v214, v248, v248
	v_fma_f32 v249, -v215, v249, v249
	v_cvt_pk_bf16_f32 v236, v246, v247
	v_cvt_pk_bf16_f32 v237, v248, v249
	s_waitcnt lgkmcnt(0)
	v_add_u32_e32 v233, v231, v244
	ds_read_b128 v[2:5], v233 offset:0
	ds_read_b128 v[6:9], v233 offset:16
	ds_read_b128 v[10:13], v233 offset:32
	ds_read_b128 v[14:17], v233 offset:48
	v_exp_f32_e32 v212, v20
	v_exp_f32_e32 v213, v24
	v_exp_f32_e32 v214, v28
	v_exp_f32_e32 v215, v32
	v_exp_f32_e32 v217, v18
	v_fma_f32 v251, v212, s12, s12
	v_exp_f32_e32 v218, v22
	v_fma_f32 v252, v213, s12, s12
	v_exp_f32_e32 v219, v26
	v_fma_f32 v253, v214, s12, s12
	v_exp_f32_e32 v220, v30
	v_fma_f32 v254, v215, s12, s12
	v_fmac_f32_e32 v251, v217, v251
	v_fmac_f32_e32 v252, v218, v252
	v_fmac_f32_e32 v253, v219, v253
	v_fmac_f32_e32 v254, v220, v254
	v_rcp_f32_e32 v217, v251
	v_rcp_f32_e32 v218, v252
	v_rcp_f32_e32 v219, v253
	v_rcp_f32_e32 v220, v254
	v_exp_f32_e32 v246, v21
	v_fma_f32 v198, -v212, v217, v217
	v_exp_f32_e32 v247, v25
	v_fma_f32 v199, -v213, v218, v218
	v_exp_f32_e32 v248, v29
	v_fma_f32 v200, -v214, v219, v219
	v_exp_f32_e32 v249, v33
	v_fma_f32 v201, -v215, v220, v220
	v_exp_f32_e32 v212, v198
	v_add_f32_e32 v246, 1.0, v246
	v_exp_f32_e32 v213, v199
	v_add_f32_e32 v247, 1.0, v247
	v_exp_f32_e32 v214, v200
	v_add_f32_e32 v248, 1.0, v248
	v_exp_f32_e32 v215, v201
	v_add_f32_e32 v249, 1.0, v249
	v_fmac_f32_e32 v246, v246, v212
	v_fmac_f32_e32 v247, v247, v213
	v_fmac_f32_e32 v248, v248, v214
	v_fmac_f32_e32 v249, v249, v215
	v_rcp_f32_e32 v246, v246
	v_rcp_f32_e32 v247, v247
	v_rcp_f32_e32 v248, v248
	v_rcp_f32_e32 v249, v249
	v_fma_f32 v246, -v212, v246, v246
	v_fma_f32 v247, -v213, v247, v247
	v_fma_f32 v248, -v214, v248, v248
	v_fma_f32 v249, -v215, v249, v249
	v_cvt_pk_bf16_f32 v238, v246, v247
	v_cvt_pk_bf16_f32 v239, v248, v249
	ds_write_b128 v211, v[236:239] offset:0
	s_waitcnt lgkmcnt(0)
	s_barrier
	ds_read_b128 v[130:133], v210 offset:0
	ds_read_b128 v[134:137], v210 offset:1024
	ds_read_b128 v[18:21], v233 offset:128
	ds_read_b128 v[22:25], v233 offset:144
	ds_read_b128 v[26:29], v233 offset:160
	ds_read_b128 v[30:33], v233 offset:176
	v_exp_f32_e32 v212, v36
	v_exp_f32_e32 v213, v40
	v_exp_f32_e32 v214, v44
	v_exp_f32_e32 v215, v48
	ds_read_b128 v[138:141], v210 offset:2048
	ds_read_b128 v[142:145], v210 offset:3072
	v_exp_f32_e32 v217, v34
	v_fma_f32 v251, v212, s12, s12
	v_exp_f32_e32 v218, v38
	v_fma_f32 v252, v213, s12, s12
	v_exp_f32_e32 v219, v42
	v_fma_f32 v253, v214, s12, s12
	v_exp_f32_e32 v220, v46
	v_fma_f32 v254, v215, s12, s12
	ds_read_b128 v[146:149], v210 offset:4096
	ds_read_b128 v[150:153], v210 offset:5120
	v_fmac_f32_e32 v251, v217, v251
	v_fmac_f32_e32 v252, v218, v252
	v_fmac_f32_e32 v253, v219, v253
	v_fmac_f32_e32 v254, v220, v254
	ds_read_b128 v[154:157], v210 offset:6144
	ds_read_b128 v[158:161], v210 offset:7168
	v_rcp_f32_e32 v217, v251
	v_rcp_f32_e32 v218, v252
	v_rcp_f32_e32 v219, v253
	v_rcp_f32_e32 v220, v254
	v_exp_f32_e32 v246, v37
	v_fma_f32 v202, -v212, v217, v217
	v_exp_f32_e32 v247, v41
	v_fma_f32 v203, -v213, v218, v218
	v_exp_f32_e32 v248, v45
	v_fma_f32 v204, -v214, v219, v219
	v_exp_f32_e32 v249, v49
	v_fma_f32 v205, -v215, v220, v220
	v_exp_f32_e32 v212, v202
	v_add_f32_e32 v246, 1.0, v246
	v_exp_f32_e32 v213, v203
	v_add_f32_e32 v247, 1.0, v247
	v_exp_f32_e32 v214, v204
	v_add_f32_e32 v248, 1.0, v248
	v_exp_f32_e32 v215, v205
	v_add_f32_e32 v249, 1.0, v249
	v_fmac_f32_e32 v246, v246, v212
	v_fmac_f32_e32 v247, v247, v213
	v_fmac_f32_e32 v248, v248, v214
	v_fmac_f32_e32 v249, v249, v215
	v_rcp_f32_e32 v246, v246
	v_rcp_f32_e32 v247, v247
	v_rcp_f32_e32 v248, v248
	v_rcp_f32_e32 v249, v249
	v_fma_f32 v246, -v212, v246, v246
	v_fma_f32 v247, -v213, v247, v247
	v_fma_f32 v248, -v214, v248, v248
	v_fma_f32 v249, -v215, v249, v249
	v_cvt_pk_bf16_f32 v236, v246, v247
	v_cvt_pk_bf16_f32 v237, v248, v249
	s_waitcnt lgkmcnt(0)
	v_mfma_f32_32x32x16_bf16 v[2:17], v[126:129], v[130:133], v[2:17]
	v_add_u32_e32 v234, v231, v245
	ds_read_b128 v[34:37], v234 offset:0
	ds_read_b128 v[38:41], v234 offset:16
	ds_read_b128 v[42:45], v234 offset:32
	ds_read_b128 v[46:49], v234 offset:48
	v_add_u32_e32 v232, 0x100, v232
	v_exp_f32_e32 v212, v84
	v_exp_f32_e32 v213, v88
	v_exp_f32_e32 v214, v92
	v_exp_f32_e32 v215, v96
	v_mfma_f32_32x32x16_bf16 v[2:17], v[122:125], v[134:137], v[2:17]
	v_exp_f32_e32 v217, v82
	v_fma_f32 v251, v212, s12, s12
	v_exp_f32_e32 v218, v86
	v_fma_f32 v252, v213, s12, s12
	v_exp_f32_e32 v219, v90
	v_fma_f32 v253, v214, s12, s12
	v_exp_f32_e32 v220, v94
	v_fma_f32 v254, v215, s12, s12
	v_mfma_f32_32x32x16_bf16 v[2:17], v[118:121], v[138:141], v[2:17]
	v_fmac_f32_e32 v251, v217, v251
	v_fmac_f32_e32 v252, v218, v252
	v_fmac_f32_e32 v253, v219, v253
	v_fmac_f32_e32 v254, v220, v254
	v_mfma_f32_32x32x16_bf16 v[2:17], v[114:117], v[142:145], v[2:17]
	v_rcp_f32_e32 v217, v251
	v_rcp_f32_e32 v218, v252
	v_rcp_f32_e32 v219, v253
	v_rcp_f32_e32 v220, v254
	v_mfma_f32_32x32x16_bf16 v[2:17], v[110:113], v[146:149], v[2:17]
	v_exp_f32_e32 v246, v85
	v_fma_f32 v206, -v212, v217, v217
	v_exp_f32_e32 v247, v89
	v_fma_f32 v207, -v213, v218, v218
	v_exp_f32_e32 v248, v93
	v_fma_f32 v208, -v214, v219, v219
	v_exp_f32_e32 v249, v97
	v_fma_f32 v209, -v215, v220, v220
	v_mfma_f32_32x32x16_bf16 v[2:17], v[106:109], v[150:153], v[2:17]
	v_mfma_f32_32x32x16_bf16 v[2:17], v[102:105], v[154:157], v[2:17]
	v_exp_f32_e32 v212, v206
	v_add_f32_e32 v246, 1.0, v246
	v_exp_f32_e32 v213, v207
	v_add_f32_e32 v247, 1.0, v247
	v_exp_f32_e32 v214, v208
	v_add_f32_e32 v248, 1.0, v248
	v_exp_f32_e32 v215, v209
	v_add_f32_e32 v249, 1.0, v249
	v_fmac_f32_e32 v246, v246, v212
	v_fmac_f32_e32 v247, v247, v213
	v_fmac_f32_e32 v248, v248, v214
	v_fmac_f32_e32 v249, v249, v215
	v_mfma_f32_32x32x16_bf16 v[2:17], v[98:101], v[158:161], v[2:17]
	v_rcp_f32_e32 v246, v246
	v_rcp_f32_e32 v247, v247
	v_rcp_f32_e32 v248, v248
	v_rcp_f32_e32 v249, v249
	v_fma_f32 v246, -v212, v246, v246
	v_fma_f32 v247, -v213, v247, v247
	v_fma_f32 v248, -v214, v248, v248
	v_fma_f32 v249, -v215, v249, v249
	v_cvt_pk_bf16_f32 v238, v246, v247
	v_cvt_pk_bf16_f32 v239, v248, v249
	ds_write_b128 v211, v[236:239] offset:8192
	s_waitcnt lgkmcnt(0)
	s_barrier
	.p2align 6
